# v66 + full grid barrier: waiting workgroups poll the top-level generation word directly (one polling hop less)
# baseline (speedup 1.0000x reference)
.LBB0_11:
	v_readlane_b32 s6, v250, 9
	s_lshl_b32 s2, s6, 3
	v_writelane_b32 v250, s2, 10
	s_lshl_b32 s72, s91, 3
	v_readlane_b32 s28, v250, 0
	s_cmpk_lt_i32 s28, 0x580
	s_cselect_b64 s[2:3], -1, 0
	v_writelane_b32 v250, s2, 11
	v_mov_b32_e32 v1, 0
	v_mov_b32_e32 v228, 0xd0000
	v_writelane_b32 v250, s3, 12
	s_mul_hi_i32 s2, s28, 0x2e8ba2e9
	s_lshr_b32 s3, s2, 31
	s_lshr_b32 s2, s2, 8
	s_add_i32 s2, s2, s3
	s_mulk_i32 s2, 0x580
	s_sub_i32 s2, s28, s2
	s_sext_i32_i16 s3, s2
	s_bfe_u32 s3, s3, 0x3001c
	s_add_i32 s3, s2, s3
	s_and_b32 s4, s3, 0xfff8
	s_sub_i32 s26, s2, s4
	s_sext_i32_i16 s2, s3
	s_ashr_i32 s22, s2, 3
	s_cmpk_lt_i32 s28, 0x100
	s_cselect_b64 s[2:3], -1, 0
	v_writelane_b32 v250, s2, 13
	v_mov_b32_e32 v196, 0x358637bd
	v_mov_b32_e32 v199, 0x260
	v_writelane_b32 v250, s3, 14
	s_ashr_i32 s2, s28, 31
	s_lshr_b32 s3, s2, 24
	s_add_i32 s3, s28, s3
	s_ashr_i32 s30, s3, 8
	s_and_b32 s3, s3, 0xffffff00
	s_sub_i32 s3, s28, s3
	s_bfe_u32 s4, s3, 0x3001c
	s_add_i32 s4, s3, s4
	s_and_b32 s5, s4, 0xfff8
	s_sub_i32 s5, s3, s5
	s_sext_i32_i16 s23, s5
	s_sext_i32_i16 s4, s4
	s_ashr_i32 s24, s4, 3
	s_lshl_b32 s25, s23, 5
	s_cmpk_lt_i32 s28, 0x300
	s_cselect_b64 s[4:5], -1, 0
	v_writelane_b32 v250, s4, 15
	v_mov_b32_e32 v225, 1
	v_mov_b32_e32 v197, 0x3000
	v_writelane_b32 v250, s5, 16
	s_ashr_i32 s4, s3, 31
	s_lshr_b32 s4, s4, 29
	s_add_i32 s4, s3, s4
	s_ashr_i32 s18, s4, 3
	s_and_b32 s4, s4, -8
	s_sub_i32 s21, s3, s4
	s_mul_hi_i32 s3, s28, 0x2aaaaaab
	s_lshr_b32 s4, s3, 31
	s_lshr_b32 s3, s3, 7
	s_add_i32 s3, s3, s4
	s_mulk_i32 s3, 0x300
	s_sub_i32 s3, s28, s3
	s_bfe_u32 s4, s3, 0x3001c
	s_add_i32 s4, s3, s4
	s_and_b32 s5, s4, 0xfff8
	s_sub_i32 s19, s3, s5
	s_sext_i32_i16 s3, s4
	s_lshl_b32 s20, s21, 5
	s_ashr_i32 s16, s3, 3
	s_cmpk_lt_i32 s28, 0x540
	s_cselect_b64 s[4:5], -1, 0
	v_writelane_b32 v250, s4, 17
	s_mul_hi_i32 s3, s28, 0x30c30c31
	s_add_i32 s13, s28, s91
	v_writelane_b32 v250, s5, 18
	s_lshr_b32 s4, s3, 31
	s_lshr_b32 s3, s3, 8
	s_add_i32 s3, s3, s4
	s_mulk_i32 s3, 0x540
	s_sub_i32 s3, s28, s3
	s_sext_i32_i16 s4, s3
	s_bfe_u32 s4, s4, 0x3001c
	s_add_i32 s4, s3, s4
	s_and_b32 s5, s4, 0xfff8
	s_sub_i32 s17, s3, s5
	s_sext_i32_i16 s3, s4
	s_ashr_i32 s15, s3, 3
	s_sub_i32 s12, s13, 64
	s_cmpk_lt_i32 s6, 0x100
	s_cselect_b64 s[4:5], -1, 0
	s_lshl_b32 s3, s6, 9
	v_writelane_b32 v250, s4, 19
	s_cmp_lt_i32 s28, 64
	v_mov_b32_e32 v234, 0x4000
	v_writelane_b32 v250, s5, 20
	s_cselect_b64 s[4:5], -1, 0
	s_lshr_b32 s2, s2, 30
	s_add_i32 s7, s28, s2
	s_and_b32 s2, s7, -4
	s_sub_i32 s2, s28, s2
	v_writelane_b32 v250, s3, 21
	s_ashr_i32 s3, s2, 31
	s_lshr_b32 s3, s3, 29
	v_writelane_b32 v250, s4, 22
	s_add_i32 s3, s2, s3
	s_ashr_i32 s27, s7, 2
	v_writelane_b32 v250, s5, 23
	s_ashr_i32 s4, s3, 3
	s_and_b32 s3, s3, -8
	s_sub_i32 s2, s2, s3
	s_min_i32 s2, s2, 4
	s_add_i32 s4, s2, s4
	s_ashr_i32 s2, s4, 31
	s_lshr_b32 s2, s2, 28
	s_add_i32 s5, s4, s2
	s_ashr_i32 s2, s5, 4
	s_and_b32 s5, s5, -16
	s_sub_i32 s6, s4, s5
	s_ashr_i32 s4, s7, 4
	s_ashr_i32 s5, s4, 31
	s_lshl_b64 s[4:5], s[4:5], 20
	v_writelane_b32 v250, s4, 24
	s_lshl_b32 s2, s2, 2
	s_sub_i32 s3, 1, s2
	v_writelane_b32 v250, s5, 25
	s_lshl_b32 s4, s27, 9
	v_writelane_b32 v250, s27, 26
	s_and_b32 s4, s4, 0x600
	v_writelane_b32 v250, s4, 27
	s_ashr_i32 s4, s7, 5
	s_ashr_i32 s5, s4, 31
	s_lshl_b64 s[4:5], s[4:5], 21
	v_writelane_b32 v250, s4, 28
	s_ashr_i32 s73, s72, 31
	s_min_i32 s3, s3, 4
	v_writelane_b32 v250, s5, 29
	s_add_i32 s7, s28, 64
	v_readlane_b32 s27, v250, 5
	s_sub_i32 s27, 0, s27
	s_lshl_b64 s[4:5], s[72:73], 8
	s_lshl_b32 s92, s91, 9
	v_writelane_b32 v250, s27, 30
	s_lshl_b32 s27, s14, 8
	s_add_u32 s10, s10, s27
	s_addc_u32 s11, s11, 0
	s_add_u32 s34, s10, 0x1400
	s_addc_u32 s35, s11, 0
	v_writelane_b32 v250, s34, 31
	s_add_u32 s10, s10, 0x2400
	s_addc_u32 s11, s11, 0
	v_writelane_b32 v250, s35, 32
	v_writelane_b32 v250, s10, 33
	v_mov_b32_e32 v230, 0x5000
	v_mov_b32_e32 v232, 0x1600
	v_writelane_b32 v250, s11, 34
	s_add_u32 s10, s8, 0x4200
	s_addc_u32 s11, s9, 0
	v_writelane_b32 v250, s10, 35
	v_mov_b32_e32 v233, 0x7f61b1e6
	s_mov_b32 s89, 0x2e8ba2e9
	v_writelane_b32 v250, s11, 36
	s_add_u32 s10, s8, 0x4400
	s_addc_u32 s11, s9, 0
	v_writelane_b32 v250, s10, 37
	s_movk_i32 s95, 0x100
	s_mov_b32 s96, 0x800000
	v_writelane_b32 v250, s11, 38
	s_add_u32 s10, s8, 0x4500
	s_addc_u32 s11, s9, 0
	v_writelane_b32 v250, s10, 39
	s_movk_i32 s90, 0xfea0
	s_movk_i32 s94, 0x2000
	v_writelane_b32 v250, s11, 40
	s_add_u32 s10, s8, 0x4600
	s_addc_u32 s11, s9, 0
	v_writelane_b32 v250, s10, 41
	s_brev_b32 s97, 1
	s_mov_b32 s81, 0
	v_writelane_b32 v250, s11, 42
	s_add_u32 s10, s8, 0x4700
	s_addc_u32 s11, s9, 0
	v_writelane_b32 v250, s10, 43
	s_mov_b64 s[70:71], 0x30000
	s_nop 0
	v_writelane_b32 v250, s11, 44
	s_add_u32 s10, s8, 0x4800
	s_addc_u32 s11, s9, 0
	v_writelane_b32 v250, s10, 45
	s_nop 1
	v_writelane_b32 v250, s11, 46
	s_add_u32 s10, s8, 0x4900
	s_addc_u32 s11, s9, 0
	v_writelane_b32 v250, s10, 47
	s_nop 1
	v_writelane_b32 v250, s11, 48
	s_add_u32 s10, s8, 0x4a00
	s_addc_u32 s11, s9, 0
	v_writelane_b32 v250, s10, 49
	s_nop 1
	v_writelane_b32 v250, s11, 50
	s_add_u32 s10, s8, 0x4b00
	s_addc_u32 s11, s9, 0
	v_writelane_b32 v250, s10, 51
	s_nop 1
	v_writelane_b32 v250, s11, 52
	s_add_u32 s10, s8, 0x4c00
	s_addc_u32 s11, s9, 0
	v_writelane_b32 v250, s10, 53
	s_nop 1
	v_writelane_b32 v250, s11, 54
	s_add_u32 s10, s8, 0x4d00
	s_addc_u32 s11, s9, 0
	v_writelane_b32 v250, s10, 55
	s_nop 1
	v_writelane_b32 v250, s11, 56
	s_add_u32 s10, s8, 0x4e00
	s_addc_u32 s11, s9, 0
	v_writelane_b32 v250, s10, 57
	s_nop 1
	v_writelane_b32 v250, s11, 58
	s_add_u32 s10, s8, 0x4f00
	s_addc_u32 s11, s9, 0
	v_writelane_b32 v250, s10, 59
	s_nop 1
	v_writelane_b32 v250, s11, 60
	s_add_u32 s10, s8, 0x5000
	s_addc_u32 s11, s9, 0
	v_writelane_b32 v250, s10, 61
	s_nop 1
	v_writelane_b32 v250, s11, 62
	s_add_u32 s10, s8, 0x5100
	s_addc_u32 s11, s9, 0
	v_writelane_b32 v250, s10, 63
	s_nop 0
	v_readlane_b32 s34, v250, 6
	v_writelane_b32 v251, s11, 0
	s_add_u32 s10, s8, 0x5200
	s_addc_u32 s11, s9, 0
	v_writelane_b32 v251, s10, 1
	s_mov_b32 s42, s34
	v_readlane_b32 s35, v250, 7
	v_writelane_b32 v251, s11, 2
	s_add_u32 s10, s8, 0x5300
	s_addc_u32 s11, s9, 0
	v_writelane_b32 v251, s10, 3
	s_cmp_eq_u32 s14, 15
	s_nop 0
	v_writelane_b32 v251, s11, 4
	s_cselect_b64 s[10:11], -1, 0
	v_writelane_b32 v251, s10, 5
	s_cmp_eq_u32 s14, 14
	s_nop 0
	v_writelane_b32 v251, s11, 6
	s_cselect_b64 s[10:11], -1, 0
	v_writelane_b32 v251, s10, 7
	s_cmp_eq_u32 s14, 13
	s_nop 0
	v_writelane_b32 v251, s11, 8
	s_cselect_b64 s[10:11], -1, 0
	v_writelane_b32 v251, s10, 9
	s_cmp_eq_u32 s14, 12
	s_nop 0
	v_writelane_b32 v251, s11, 10
	s_cselect_b64 s[10:11], -1, 0
	v_writelane_b32 v251, s10, 11
	s_cmp_eq_u32 s14, 11
	s_nop 0
	v_writelane_b32 v251, s11, 12
	s_cselect_b64 s[10:11], -1, 0
	v_writelane_b32 v251, s10, 13
	s_cmp_eq_u32 s14, 10
	s_nop 0
	v_writelane_b32 v251, s11, 14
	s_cselect_b64 s[10:11], -1, 0
	v_writelane_b32 v251, s10, 15
	s_cmp_eq_u32 s14, 9
	s_nop 0
	v_writelane_b32 v251, s11, 16
	s_cselect_b64 s[10:11], -1, 0
	v_writelane_b32 v251, s10, 17
	s_cmp_eq_u32 s14, 8
	s_nop 0
	v_writelane_b32 v251, s11, 18
	s_cselect_b64 s[10:11], -1, 0
	v_writelane_b32 v251, s10, 19
	s_cmp_eq_u32 s14, 7
	s_nop 0
	v_writelane_b32 v251, s11, 20
	s_cselect_b64 s[10:11], -1, 0
	v_writelane_b32 v251, s10, 21
	s_cmp_eq_u32 s14, 6
	s_nop 0
	v_writelane_b32 v251, s11, 22
	s_cselect_b64 s[10:11], -1, 0
	v_writelane_b32 v251, s10, 23
	s_cmp_eq_u32 s14, 5
	s_nop 0
	v_writelane_b32 v251, s11, 24
	s_cselect_b64 s[10:11], -1, 0
	v_writelane_b32 v251, s10, 25
	s_cmp_eq_u32 s14, 4
	s_nop 0
	v_writelane_b32 v251, s11, 26
	s_cselect_b64 s[10:11], -1, 0
	v_writelane_b32 v251, s10, 27
	s_cmp_eq_u32 s14, 3
	s_nop 0
	v_writelane_b32 v251, s11, 28
	s_cselect_b64 s[10:11], -1, 0
	v_writelane_b32 v251, s10, 29
	s_cmp_eq_u32 s14, 2
	s_nop 0
	v_writelane_b32 v251, s11, 30
	s_cselect_b64 s[10:11], -1, 0
	v_writelane_b32 v251, s10, 31
	s_cmp_eq_u32 s14, 1
	s_nop 0
	v_writelane_b32 v251, s11, 32
	s_cselect_b64 s[10:11], -1, 0
	v_writelane_b32 v251, s10, 33
	s_cmp_eq_u32 s14, 0
	s_nop 0
	v_writelane_b32 v251, s11, 34
	s_cselect_b64 s[10:11], -1, 0
	v_writelane_b32 v251, s10, 35
	s_nop 1
	v_writelane_b32 v251, s11, 36
	s_add_u32 s10, s8, 0x7400
	s_addc_u32 s11, s9, 0
	v_writelane_b32 v251, s10, 37
	s_nop 1
	v_writelane_b32 v251, s11, 38
	s_add_u32 s10, s8, 0x7500
	s_addc_u32 s11, s9, 0
	v_writelane_b32 v251, s10, 39
	s_nop 1
	v_writelane_b32 v251, s11, 40
	s_add_i32 s10, s34, 1
	s_add_u32 s8, s8, 0x4300
	v_writelane_b32 v251, s10, 41
	s_addc_u32 s9, s9, 0
	v_writelane_b32 v251, s8, 42
	s_nop 1
	v_writelane_b32 v251, s9, 43
	s_and_b32 s8, s28, 7
	s_cmp_eq_u32 s14, s8
	s_cselect_b64 s[10:11], -1, 0
	v_writelane_b32 v251, s10, 44
	s_cmp_lg_u32 s14, s8
	s_sext_i32_i16 s8, s26
	v_writelane_b32 v251, s11, 45
	s_cselect_b64 s[10:11], -1, 0
	v_writelane_b32 v251, s10, 46
	s_ashr_i32 s9, s91, 3
	s_cmp_lt_i32 s8, 0
	v_writelane_b32 v251, s11, 47
	v_writelane_b32 v251, s9, 48
	s_movk_i32 s9, 0xb1
	s_cselect_b32 s9, s9, 0xb0
	s_mul_i32 s8, s9, s8
	s_add_i32 s8, s8, s22
	s_mul_hi_i32 s9, s8, 0x2e8ba2e9
	s_lshr_b32 s10, s9, 31
	s_ashr_i32 s9, s9, 4
	s_add_i32 s9, s9, s10
	s_mul_i32 s10, s9, 0x58
	s_lshl_b32 s22, s9, 2
	s_sub_i32 s14, s8, s10
	s_sub_i32 s8, 64, s22
	s_min_i32 s26, s8, 4
	s_cmp_lt_i32 s23, 0
	s_mul_i32 s23, s23, 33
	s_cselect_b32 s8, s23, s25
	s_add_i32 s8, s8, s24
	s_ashr_i32 s9, s8, 31
	s_lshr_b32 s9, s9, 28
	s_add_i32 s9, s8, s9
	s_and_b32 s10, s9, -16
	s_sub_i32 s23, s8, s10
	s_ashr_i32 s8, s9, 4
	s_lshl_b32 s24, s8, 2
	s_sub_i32 s8, 64, s24
	s_min_i32 s25, s8, 4
	s_cmp_lt_i32 s21, 0
	s_mul_i32 s21, s21, 33
	s_cselect_b32 s8, s21, s20
	s_add_i32 s8, s8, s18
	s_ashr_i32 s9, s8, 31
	s_lshr_b32 s9, s9, 28
	s_add_i32 s9, s8, s9
	s_and_b32 s10, s9, -16
	s_ashr_i32 s31, s30, 31
	s_sub_i32 s18, s8, s10
	s_lshl_b64 s[10:11], s[30:31], 24
	s_ashr_i32 s9, s9, 4
	v_writelane_b32 v251, s10, 49
	s_sext_i32_i16 s8, s19
	s_lshl_b32 s19, s9, 2
	v_writelane_b32 v251, s11, 50
	s_mov_b32 s10, s30
	s_sub_i32 s9, 64, s19
	v_writelane_b32 v251, s10, 51
	s_min_i32 s20, s9, 4
	s_movk_i32 s9, 0x61
	v_writelane_b32 v251, s11, 52
	s_lshl_b64 s[10:11], s[30:31], 20
	s_cmp_lt_i32 s8, 0
	s_cselect_b32 s9, s9, 0x60
	s_mul_i32 s8, s9, s8
	s_add_i32 s8, s8, s16
	v_writelane_b32 v251, s10, 53
	s_mul_hi_i32 s9, s8, 0x2aaaaaab
	s_nop 0
	v_writelane_b32 v251, s11, 54
	s_lshr_b32 s10, s9, 31
	s_ashr_i32 s9, s9, 3
	s_add_i32 s9, s9, s10
	s_mul_i32 s10, s9, 48
	s_lshl_b32 s9, s9, 2
	s_sub_i32 s16, s8, s10
	s_sub_i32 s10, 64, s9
	s_sext_i32_i16 s8, s17
	s_min_i32 s17, s10, 4
	s_cmp_lt_i32 s8, 0
	s_movk_i32 s10, 0xa9
	s_cselect_b32 s10, s10, 0xa8
	s_mul_i32 s8, s10, s8
	s_add_i32 s8, s8, s15
	s_abs_i32 s15, s26
	v_cvt_f32_u32_e32 v0, s15
	s_mul_hi_i32 s10, s8, 0x30c30c31
	s_lshr_b32 s11, s10, 31
	s_ashr_i32 s10, s10, 4
	v_rcp_iflag_f32_e32 v0, v0
	s_add_i32 s10, s10, s11
	s_mul_i32 s11, s10, 0x54
	s_sub_i32 s8, s8, s11
	v_mul_f32_e32 v0, 0x4f7ffffe, v0
	v_cvt_u32_f32_e32 v0, v0
	s_sub_i32 s11, 0, s15
	s_lshl_b32 s10, s10, 2
	s_xor_b32 s28, s14, s26
	v_readfirstlane_b32 s21, v0
	s_mul_i32 s11, s11, s21
	s_mul_hi_u32 s11, s21, s11
	s_add_i32 s21, s21, s11
	s_abs_i32 s11, s14
	s_mul_hi_u32 s21, s11, s21
	s_mul_i32 s27, s21, s15
	s_sub_i32 s27, s11, s27
	s_sub_i32 s11, 64, s10
	s_min_i32 s11, s11, 4
	s_ashr_i32 s28, s28, 31
	s_add_i32 s29, s21, 1
	s_sub_i32 s30, s27, s15
	s_cmp_ge_u32 s27, s15
	s_cselect_b32 s21, s29, s21
	s_cselect_b32 s27, s30, s27
	s_add_i32 s29, s21, 1
	s_cmp_ge_u32 s27, s15
	s_cselect_b32 s15, s29, s21
	s_xor_b32 s15, s15, s28
	s_sub_i32 s30, s15, s28
	s_mul_i32 s15, s30, s26
	s_sub_i32 s14, s14, s15
	s_abs_i32 s15, s25
	v_cvt_f32_u32_e32 v0, s15
	s_add_i32 s36, s22, s14
	s_sub_i32 s21, 0, s15
	s_lshl_b32 s22, s36, 8
	v_rcp_iflag_f32_e32 v0, v0
	v_writelane_b32 v251, s22, 55
	s_mov_b32 s28, s36
	s_ashr_i32 s37, s36, 31
	v_mul_f32_e32 v0, 0x4f7ffffe, v0
	v_cvt_u32_f32_e32 v0, v0
	v_writelane_b32 v251, s28, 56
	s_ashr_i32 s31, s30, 31
	s_xor_b32 s14, s23, s25
	v_readfirstlane_b32 s26, v0
	s_mul_i32 s21, s21, s26
	s_mul_hi_u32 s21, s26, s21
	s_add_i32 s26, s26, s21
	s_abs_i32 s21, s23
	v_writelane_b32 v251, s29, 57
	s_lshl_b64 s[28:29], s[36:37], 19
	s_mul_hi_u32 s26, s21, s26
	v_writelane_b32 v251, s28, 58
	s_mul_i32 s27, s26, s15
	s_sub_i32 s21, s21, s27
	v_writelane_b32 v251, s29, 59
	s_mov_b32 s28, s30
	v_writelane_b32 v251, s28, 60
	s_ashr_i32 s14, s14, 31
	s_add_i32 s22, s26, 1
	s_sub_i32 s27, s21, s15
	v_writelane_b32 v251, s29, 61
	s_lshl_b64 s[28:29], s[30:31], 19
	s_cmp_ge_u32 s21, s15
	s_cselect_b32 s22, s22, s26
	s_cselect_b32 s21, s27, s21
	s_add_i32 s26, s22, 1
	s_cmp_ge_u32 s21, s15
	s_cselect_b32 s15, s26, s22
	s_abs_i32 s21, s20
	v_cvt_f32_u32_e32 v0, s21
	v_writelane_b32 v251, s28, 62
	s_xor_b32 s15, s15, s14
	v_rcp_iflag_f32_e32 v0, v0
	v_writelane_b32 v251, s29, 63
	s_sub_i32 s28, s15, s14
	s_sub_i32 s15, 0, s21
	v_mul_f32_e32 v0, 0x4f7ffffe, v0
	v_cvt_u32_f32_e32 v0, v0
	s_mul_i32 s14, s28, s25
	s_sub_i32 s14, s23, s14
	s_add_i32 s30, s24, s14
	v_readfirstlane_b32 s22, v0
	s_mul_i32 s15, s15, s22
	s_mul_hi_u32 s15, s22, s15
	s_add_i32 s22, s22, s15
	s_abs_i32 s15, s18
	s_mul_hi_u32 s22, s15, s22
	s_mul_i32 s23, s22, s21
	s_ashr_i32 s14, s30, 5
	s_sub_i32 s23, s15, s23
	s_ashr_i32 s15, s14, 31
	s_lshl_b64 s[14:15], s[14:15], 21
	v_writelane_b32 v252, s14, 0
	s_mov_b32 s26, s30
	s_ashr_i32 s31, s30, 31
	v_writelane_b32 v252, s15, 1
	s_lshl_b32 s15, s30, 8
	v_writelane_b32 v252, s15, 2
	v_writelane_b32 v252, s26, 3
	s_ashr_i32 s29, s28, 31
	s_xor_b32 s14, s18, s20
	v_writelane_b32 v252, s27, 4
	s_lshl_b64 s[26:27], s[30:31], 19
	v_writelane_b32 v252, s26, 5
	s_ashr_i32 s14, s14, 31
	s_add_i32 s15, s22, 1
	v_writelane_b32 v252, s27, 6
	s_mov_b32 s26, s28
	v_writelane_b32 v252, s26, 7
	s_sub_i32 s24, s23, s21
	s_nop 0
	v_writelane_b32 v252, s27, 8
	s_lshl_b64 s[26:27], s[28:29], 19
	s_cmp_ge_u32 s23, s21
	s_cselect_b32 s15, s15, s22
	s_cselect_b32 s22, s24, s23
	s_add_i32 s23, s15, 1
	s_cmp_ge_u32 s22, s21
	s_cselect_b32 s15, s23, s15
	v_writelane_b32 v252, s26, 9
	s_xor_b32 s15, s15, s14
	s_sub_i32 s14, s15, s14
	v_writelane_b32 v252, s27, 10
	v_writelane_b32 v252, s14, 11
	s_mul_i32 s14, s14, s20
	s_sub_i32 s14, s18, s14
	s_add_i32 s14, s19, s14
	v_writelane_b32 v252, s14, 12
	s_abs_i32 s14, s17
	v_cvt_f32_u32_e32 v0, s14
	s_sub_i32 s15, 0, s14
	s_mov_b32 s26, 0x3db8aa3b
	v_rcp_iflag_f32_e32 v0, v0
	s_nop 0
	v_mul_f32_e32 v0, 0x4f7ffffe, v0
	v_cvt_u32_f32_e32 v0, v0
	s_nop 0
	v_readfirstlane_b32 s18, v0
	s_mul_i32 s15, s15, s18
	s_mul_hi_u32 s15, s18, s15
	s_add_i32 s18, s18, s15
	s_abs_i32 s15, s16
	s_mul_hi_u32 s18, s15, s18
	s_mul_i32 s19, s18, s14
	s_sub_i32 s15, s15, s19
	s_xor_b32 s19, s16, s17
	s_ashr_i32 s19, s19, 31
	s_add_i32 s20, s18, 1
	s_sub_i32 s21, s15, s14
	s_cmp_ge_u32 s15, s14
	s_cselect_b32 s18, s20, s18
	s_cselect_b32 s15, s21, s15
	s_add_i32 s20, s18, 1
	s_cmp_ge_u32 s15, s14
	s_cselect_b32 s14, s20, s18
	s_abs_i32 s33, s72
	v_cvt_f32_u32_e32 v0, s33
	s_xor_b32 s14, s14, s19
	s_sub_i32 s22, s14, s19
	s_mul_i32 s14, s22, s17
	v_rcp_iflag_f32_e32 v0, v0
	s_sub_i32 s14, s16, s14
	s_sub_i32 s15, 0, s33
	s_add_i32 s24, s9, s14
	v_mul_f32_e32 v0, 0x4f7ffffe, v0
	v_cvt_u32_f32_e32 v0, v0
	s_lshl_b32 s14, s24, 8
	v_writelane_b32 v252, s14, 13
	s_mov_b32 s20, s24
	v_readfirstlane_b32 s16, v0
	s_mul_i32 s15, s15, s16
	s_mul_hi_u32 s15, s16, s15
	s_add_i32 s27, s16, s15
	s_abs_i32 s15, s11
	v_cvt_f32_u32_e32 v0, s15
	s_sub_i32 s16, 0, s15
	s_ashr_i32 s25, s24, 31
	v_writelane_b32 v252, s20, 14
	v_rcp_iflag_f32_e32 v0, v0
	s_ashr_i32 s23, s22, 31
	v_writelane_b32 v252, s21, 15
	s_lshl_b64 s[20:21], s[24:25], 19
	v_mul_f32_e32 v0, 0x4f7ffffe, v0
	v_cvt_u32_f32_e32 v0, v0
	v_writelane_b32 v252, s20, 16
	s_xor_b32 s9, s8, s11
	s_ashr_i32 s9, s9, 31
	v_readfirstlane_b32 s17, v0
	s_mul_i32 s16, s16, s17
	s_mul_hi_u32 s16, s17, s16
	s_add_i32 s17, s17, s16
	s_abs_i32 s16, s8
	s_mul_hi_u32 s17, s16, s17
	s_mul_i32 s18, s17, s15
	v_writelane_b32 v252, s21, 17
	s_mov_b32 s20, s22
	s_sub_i32 s16, s16, s18
	v_writelane_b32 v252, s20, 18
	s_bfe_i32 s14, s91, 0x1001c
	s_add_i32 s18, s17, 1
	s_sub_i32 s19, s16, s15
	v_writelane_b32 v252, s21, 19
	s_lshl_b64 s[20:21], s[22:23], 19
	s_cmp_ge_u32 s16, s15
	s_cselect_b32 s17, s18, s17
	s_cselect_b32 s16, s19, s16
	s_add_i32 s18, s17, 1
	s_cmp_ge_u32 s16, s15
	s_cselect_b32 s15, s18, s17
	v_writelane_b32 v252, s20, 20
	s_xor_b32 s15, s15, s9
	s_sub_i32 s9, s15, s9
	v_writelane_b32 v252, s21, 21
	v_writelane_b32 v252, s9, 22
	s_mul_i32 s9, s9, s11
	s_sub_i32 s8, s8, s9
	s_abs_i32 s9, s91
	v_cvt_f32_u32_e32 v0, s9
	s_add_i32 s8, s10, s8
	v_writelane_b32 v252, s8, 23
	s_sub_i32 s8, 0, s9
	v_rcp_iflag_f32_e32 v0, v0
	s_mov_b64 s[20:21], 0x40000
	s_mov_b64 s[22:23], 0x50000
	s_mov_b64 s[24:25], 0x20000
	v_mul_f32_e32 v0, 0x4f7ffffe, v0
	v_cvt_u32_f32_e32 v0, v0
	s_nop 0
	v_readfirstlane_b32 s10, v0
	s_mul_i32 s8, s8, s10
	s_mul_hi_u32 s8, s10, s8
	s_add_i32 s10, s10, s8
	s_sub_i32 s8, 64, s13
	s_max_i32 s8, s12, s8
	s_mul_hi_u32 s11, s8, s10
	s_mul_i32 s11, s11, s9
	s_sub_i32 s8, s8, s11
	s_ashr_i32 s11, s12, 31
	s_sub_i32 s12, s8, s9
	s_cmp_ge_u32 s8, s9
	s_cselect_b32 s8, s12, s8
	s_sub_i32 s12, s8, s9
	s_cmp_ge_u32 s8, s9
	s_cselect_b32 s8, s12, s8
	s_xor_b32 s8, s8, s11
	s_sub_i32 s12, s8, s11
	s_cmp_lt_i32 s12, 32
	s_cselect_b64 s[16:17], -1, 0
	s_ashr_i32 s8, s12, 31
	s_lshr_b32 s8, s8, 28
	s_add_i32 s11, s12, s8
	v_writelane_b32 v252, s16, 24
	s_and_b32 s8, s11, -16
	s_sub_i32 s8, s12, s8
	v_writelane_b32 v252, s17, 25
	v_writelane_b32 v252, s12, 26
	s_ashr_i32 s12, s8, 31
	s_lshr_b32 s12, s12, 29
	s_add_i32 s12, s8, s12
	s_and_b32 s13, s12, -8
	s_sub_i32 s8, s8, s13
	s_ashr_i32 s12, s12, 3
	s_ashr_i32 s18, s11, 4
	s_cmp_gt_i32 s8, -1
	v_writelane_b32 v252, s12, 27
	s_cselect_b64 s[12:13], -1, 0
	v_writelane_b32 v252, s12, 28
	s_ashr_i32 s19, s18, 31
	s_lshl_b64 s[16:17], s[18:19], 20
	v_writelane_b32 v252, s13, 29
	s_lshl_b32 s13, s8, 1
	v_writelane_b32 v252, s13, 30
	s_lshr_b32 s11, s27, 18
	v_writelane_b32 v252, s16, 31
	s_mul_i32 s12, s11, s33
	s_sub_i32 s12, 0x4000, s12
	v_writelane_b32 v252, s17, 32
	s_mov_b32 s16, s18
	v_writelane_b32 v252, s16, 33
	s_add_i32 s13, s11, 1
	s_sub_i32 s15, s12, s33
	v_writelane_b32 v252, s17, 34
	s_lshl_b64 s[16:17], s[18:19], 22
	s_cmp_ge_u32 s12, s33
	s_cselect_b32 s11, s13, s11
	s_cselect_b32 s12, s15, s12
	s_add_i32 s13, s11, 1
	s_cmp_ge_u32 s12, s33
	s_cselect_b32 s11, s13, s11
	v_writelane_b32 v252, s16, 35
	s_xor_b32 s11, s11, s14
	s_sub_i32 s11, s11, s14
	v_writelane_b32 v252, s17, 36
	v_writelane_b32 v252, s11, 37
	s_cmp_gt_i32 s11, 0
	s_mul_hi_u32 s11, s27, 0x300
	s_mul_i32 s11, s11, s33
	s_cselect_b64 s[12:13], -1, 0
	v_writelane_b32 v252, s12, 38
	s_sub_i32 s11, 0x300, s11
	s_mov_b64 s[18:19], 0x80
	v_writelane_b32 v252, s13, 39
	s_sub_i32 s12, s11, s33
	s_cmp_ge_u32 s11, s33
	s_cselect_b32 s11, s12, s11
	s_sub_i32 s12, s11, s33
	s_cmp_ge_u32 s11, s33
	s_cselect_b32 s11, s12, s11
	v_writelane_b32 v252, s11, 40
	s_addk_i32 s11, 0x300
	s_abs_i32 s12, s11
	s_mul_hi_u32 s13, s12, s27
	s_mul_i32 s13, s13, s33
	s_sub_i32 s12, s12, s13
	s_ashr_i32 s11, s11, 31
	s_sub_i32 s13, s12, s33
	s_cmp_ge_u32 s12, s33
	s_cselect_b32 s12, s13, s12
	s_sub_i32 s13, s12, s33
	s_cmp_ge_u32 s12, s33
	s_cselect_b32 s12, s13, s12
	s_xor_b32 s12, s12, s11
	s_sub_i32 s11, s12, s11
	v_writelane_b32 v252, s11, 41
	s_addk_i32 s11, 0x100
	s_abs_i32 s12, s11
	s_mul_hi_u32 s13, s12, s27
	s_mul_i32 s13, s13, s33
	s_sub_i32 s12, s12, s13
	s_ashr_i32 s11, s11, 31
	s_sub_i32 s13, s12, s33
	s_cmp_ge_u32 s12, s33
	s_cselect_b32 s12, s13, s12
	s_sub_i32 s13, s12, s33
	s_cmp_ge_u32 s12, s33
	s_cselect_b32 s12, s13, s12
	s_xor_b32 s12, s12, s11
	s_sub_i32 s11, s12, s11
	v_writelane_b32 v252, s11, 42
	s_addk_i32 s11, 0x100
	s_abs_i32 s12, s11
	s_mul_hi_u32 s13, s12, s27
	s_mul_i32 s13, s13, s33
	s_sub_i32 s12, s12, s13
	s_ashr_i32 s11, s11, 31
	s_sub_i32 s13, s12, s33
	s_cmp_ge_u32 s12, s33
	s_cselect_b32 s12, s13, s12
	s_sub_i32 s13, s12, s33
	s_cmp_ge_u32 s12, s33
	s_cselect_b32 s12, s13, s12
	s_xor_b32 s12, s12, s11
	s_sub_i32 s11, s12, s11
	v_writelane_b32 v252, s11, 43
	s_abs_i32 s11, s3
	v_cvt_f32_u32_e32 v0, s11
	s_sub_i32 s12, 0, s11
	v_rcp_iflag_f32_e32 v0, v0
	s_nop 0
	v_mul_f32_e32 v0, 0x4f7ffffe, v0
	v_cvt_u32_f32_e32 v0, v0
	s_nop 0
	v_readfirstlane_b32 s13, v0
	s_mul_i32 s12, s12, s13
	s_mul_hi_u32 s12, s13, s12
	s_add_i32 s13, s13, s12
	s_abs_i32 s12, s6
	s_mul_hi_u32 s13, s12, s13
	s_mul_i32 s14, s13, s11
	s_sub_i32 s12, s12, s14
	s_xor_b32 s14, s6, s3
	s_ashr_i32 s14, s14, 31
	s_add_i32 s15, s13, 1
	s_sub_i32 s16, s12, s11
	s_cmp_ge_u32 s12, s11
	s_cselect_b32 s13, s15, s13
	s_cselect_b32 s12, s16, s12
	s_add_i32 s15, s13, 1
	s_cmp_ge_u32 s12, s11
	s_cselect_b32 s11, s15, s13
	s_xor_b32 s11, s11, s14
	s_sub_i32 s12, s11, s14
	s_mul_i32 s3, s12, s3
	s_sub_i32 s3, s6, s3
	s_add_i32 s2, s3, s2
	v_writelane_b32 v252, s2, 44
	s_abs_i32 s2, s7
	s_mul_hi_u32 s3, s2, s10
	s_mul_i32 s3, s3, s9
	s_mov_b32 s10, s12
	s_sub_i32 s2, s2, s3
	s_ashr_i32 s13, s12, 31
	v_writelane_b32 v252, s10, 45
	s_ashr_i32 s3, s7, 31
	s_sub_i32 s6, s2, s9
	v_writelane_b32 v252, s11, 46
	s_lshl_b64 s[10:11], s[12:13], 19
	s_cmp_ge_u32 s2, s9
	s_cselect_b32 s2, s6, s2
	s_sub_i32 s6, s2, s9
	s_cmp_ge_u32 s2, s9
	s_cselect_b32 s2, s6, s2
	s_xor_b32 s2, s2, s3
	s_sub_i32 s3, s2, s3
	v_writelane_b32 v252, s10, 47
	s_cmp_lt_i32 s3, 64
	s_cselect_b64 s[6:7], -1, 0
	v_writelane_b32 v252, s11, 48
	s_ashr_i32 s2, s3, 31
	v_writelane_b32 v252, s6, 49
	s_lshr_b32 s2, s2, 30
	s_nop 0
	v_writelane_b32 v252, s7, 50
	s_add_i32 s6, s3, s2
	s_and_b32 s2, s6, -4
	s_sub_i32 s2, s3, s2
	v_writelane_b32 v252, s3, 51
	s_ashr_i32 s3, s2, 31
	s_lshr_b32 s3, s3, 29
	s_add_i32 s3, s2, s3
	s_and_b32 s7, s3, -8
	s_sub_i32 s2, s2, s7
	s_ashr_i32 s3, s3, 3
	s_min_i32 s2, s2, 4
	s_add_i32 s2, s2, s3
	s_ashr_i32 s3, s2, 31
	s_lshr_b32 s3, s3, 30
	s_add_i32 s3, s2, s3
	s_and_b32 s3, s3, -4
	s_sub_i32 s7, 4, s3
	s_min_i32 s7, s7, 4
	s_abs_i32 s9, s7
	v_cvt_f32_u32_e32 v0, s9
	s_sub_i32 s10, 0, s9
	s_sub_i32 s2, s2, s3
	s_ashr_i32 s15, s6, 2
	v_rcp_iflag_f32_e32 v0, v0
	s_nop 0
	v_mul_f32_e32 v0, 0x4f7ffffe, v0
	v_cvt_u32_f32_e32 v0, v0
	s_nop 0
	v_readfirstlane_b32 s11, v0
	s_mul_i32 s10, s10, s11
	s_mul_hi_u32 s10, s11, s10
	s_add_i32 s11, s11, s10
	s_abs_i32 s10, s2
	s_mul_hi_u32 s11, s10, s11
	s_mul_i32 s12, s11, s9
	s_sub_i32 s10, s10, s12
	s_xor_b32 s12, s2, s7
	s_ashr_i32 s12, s12, 31
	s_add_i32 s13, s11, 1
	s_sub_i32 s14, s10, s9
	s_cmp_ge_u32 s10, s9
	s_cselect_b32 s11, s13, s11
	s_cselect_b32 s10, s14, s10
	s_add_i32 s13, s11, 1
	s_cmp_ge_u32 s10, s9
	s_cselect_b32 s9, s13, s11
	s_xor_b32 s9, s9, s12
	s_sub_i32 s9, s9, s12
	s_mul_i32 s7, s9, s7
	s_sub_i32 s2, s2, s7
	s_mul_i32 s7, s8, 3
	s_add_i32 s8, s2, s3
	s_ashr_i32 s2, s6, 5
	v_writelane_b32 v252, s9, 52
	s_ashr_i32 s3, s2, 31
	v_writelane_b32 v252, s7, 53
	s_lshl_b64 s[2:3], s[2:3], 21
	v_writelane_b32 v252, s2, 54
	s_ashr_i32 s9, s8, 31
	v_mbcnt_lo_u32_b32 v0, -1, 0
	v_writelane_b32 v252, s3, 55
	s_lshl_b32 s2, s15, 9
	v_writelane_b32 v252, s15, 56
	s_and_b32 s2, s2, 0x600
	v_writelane_b32 v252, s2, 57
	s_ashr_i32 s2, s6, 4
	s_ashr_i32 s3, s2, 31
	s_lshl_b64 s[2:3], s[2:3], 20
	v_writelane_b32 v252, s2, 58
	v_mbcnt_hi_u32_b32 v231, -1, v0
	s_mov_b32 s10, 0x8000
	v_writelane_b32 v252, s3, 59
	s_mov_b32 s2, s8
	v_writelane_b32 v252, s2, 60
	s_mov_b32 s11, 0x8120
	s_mov_b32 s7, 0xf800000
	v_writelane_b32 v252, s3, 61
	s_lshl_b64 s[2:3], s[8:9], 19
	v_writelane_b32 v252, s2, 62
	s_nop 1
	v_writelane_b32 v252, s3, 63
	v_readlane_b32 s2, v250, 3
	v_readlane_b32 s3, v250, 4
	s_load_dwordx4 s[12:15], s[2:3], 0xa0
	s_waitcnt lgkmcnt(0)
	s_add_u32 s6, s14, 0x2200400
	v_writelane_b32 v253, s6, 0
	s_addc_u32 s6, s15, 0
	v_writelane_b32 v253, s6, 1
	s_add_u32 s2, s2, 40
	v_writelane_b32 v253, s2, 2
	s_addc_u32 s2, s3, 0
	v_writelane_b32 v253, s2, 3
	s_add_u32 s2, s14, 0xf000c
	v_writelane_b32 v253, s2, 4
	s_addc_u32 s2, s15, 0
	v_writelane_b32 v253, s2, 5
	s_add_u32 s2, s14, 0xf0004
	v_writelane_b32 v253, s2, 6
	s_addc_u32 s2, s15, 0
	v_writelane_b32 v253, s2, 7
	s_lshl_b32 s2, s91, 6
	v_writelane_b32 v253, s2, 8
	s_add_u32 s2, s14, 0xeb00000
	v_writelane_b32 v253, s2, 9
	s_addc_u32 s2, s15, 0
	s_lshl_b64 s[68:69], s[72:73], 10
	v_writelane_b32 v253, s2, 10
	s_add_u32 s2, s14, 0x2200000
	v_writelane_b32 v253, s2, 11
	s_addc_u32 s2, s15, 0
	s_lshl_b32 s28, s91, 8
	s_lshl_b64 s[8:9], s[72:73], 9
	s_lshl_b64 s[76:77], s[72:73], 12
	v_writelane_b32 v253, s2, 12
	s_add_u32 s2, s14, 0x3200400
	v_writelane_b32 v253, s2, 13
	s_addc_u32 s2, s15, 0
	s_lshl_b64 s[78:79], s[72:73], 11
	v_writelane_b32 v253, s2, 14
	s_add_u32 s2, s14, 0x30000
	v_writelane_b32 v253, s2, 15
	v_writelane_b32 v253, s12, 16
	s_addc_u32 s2, s15, 0
	s_xor_b64 s[0:1], s[0:1], -1
	v_writelane_b32 v253, s13, 17
	v_writelane_b32 v253, s14, 18
	v_writelane_b32 v253, s15, 19
	v_writelane_b32 v253, s2, 20
	v_writelane_b32 v253, s0, 21
	s_ashr_i32 s93, s92, 31
	s_lshl_b32 s43, s91, 4
	v_writelane_b32 v253, s1, 22
	s_movk_i32 s3, 0x5800
	s_lshl_b64 s[0:1], s[92:93], 4
	v_writelane_b32 v253, s0, 23
	s_movk_i32 s2, 0x1600
	s_mov_b32 s6, 0xff800000
	v_writelane_b32 v253, s1, 24
	s_mov_b64 s[0:1], 0
	v_writelane_b32 v253, s0, 25
	s_mov_b32 s73, 0x42700000
	s_mov_b64 s[12:13], 0x10000
	v_writelane_b32 v253, s1, 26
	v_writelane_b32 v253, s91, 27
	s_mov_b32 s0, s92
	v_writelane_b32 v253, s0, 28
	s_nop 1
	v_writelane_b32 v253, s1, 29
	v_writelane_b32 v253, s43, 30
	s_mov_b32 s101, 0
	s_branch .LBB0_17

.LBB0_1019:
	v_readlane_b32 s14, v250, 31
	v_readlane_b32 s15, v250, 32
	v_cvt_f32_u32_e32 v0, v3
	v_sub_u32_e32 v5, 0, v3
	v_rcp_iflag_f32_e32 v0, v0
	s_nop 1
	global_atomic_add v4, v1, v225, s[14:15] sc0
	v_mul_f32_e32 v0, 0x4f7ffffe, v0
	v_cvt_u32_f32_e32 v0, v0
	v_mul_lo_u32 v5, v5, v0
	v_mul_hi_u32 v5, v0, v5
	v_add_u32_e32 v0, v0, v5
	s_waitcnt vmcnt(0)
	v_mul_hi_u32 v0, v4, v0
	v_mul_lo_u32 v5, v0, v3
	v_sub_u32_e32 v5, v4, v5
	v_add_u32_e32 v6, 1, v0
	v_cmp_ge_u32_e32 vcc, v5, v3
	v_add_u32_e32 v4, 1, v4
	s_nop 0
	v_cndmask_b32_e32 v0, v0, v6, vcc
	v_sub_u32_e32 v6, v5, v3
	v_cndmask_b32_e32 v5, v5, v6, vcc
	v_add_u32_e32 v6, 1, v0
	v_cmp_ge_u32_e32 vcc, v5, v3
	s_nop 1
	v_cndmask_b32_e32 v0, v0, v6, vcc
	v_mul_lo_u32 v5, v3, v0
	v_add_u32_e32 v3, v5, v3
	v_cmp_ne_u32_e32 vcc, v4, v3
	s_and_saveexec_b64 s[14:15], vcc
	s_xor_b64 s[14:15], exec, s[14:15]
	s_cbranch_execz .LBB0_1033
	buffer_inv sc1
	v_mov_b32_e32 v0, s101
	v_readlane_b32 s16, v251, 39
	v_readlane_b32 s17, v251, 40
	s_waitcnt lgkmcnt(0)
	s_nop 3
	global_load_dword v2, v1, s[16:17] sc1
	s_waitcnt vmcnt(0)
	v_cmp_eq_u32_e32 vcc, v2, v0
	s_and_saveexec_b64 s[16:17], vcc
	s_cbranch_execz .LBB0_1032
	s_mov_b32 s29, 1
	s_mov_b64 s[30:31], 0
	s_branch .LBB0_1023

.LBB0_2078:
	s_or_b64 exec, exec, s[0:1]
	s_waitcnt lgkmcnt(0)
	s_barrier
	s_add_i32 s101, s101, 1
	s_branch .LBB0_2096
